# RG-LRU: each direction's first A tile is requested before waiting for the weight fragments and biases
# speedup vs baseline: 1.0022x; 1.0022x over previous
.LBB0_1451:
	s_load_dwordx4 s[0:3], s[8:9], 0x138
	s_waitcnt lgkmcnt(0)
	s_mov_b64 s[4:5], s[0:1]
	s_cmp_lt_i32 s4, 12
	s_cselect_b64 s[0:1], -1, 0
	s_cmp_gt_i32 s5, 11
	s_cselect_b64 s[2:3], -1, 0
	s_and_b64 s[0:1], s[0:1], s[2:3]
	s_andn2_b64 vcc, exec, s[0:1]
	s_cbranch_vccnz .LBB0_1535
	s_mov_b64 s[24:25], s[8:9]
	v_mbcnt_lo_u32_b32 v202, -1, 0
	v_mbcnt_hi_u32_b32 v202, -1, v202
	s_load_dword s0, s[8:9], 0x148
	s_waitcnt lgkmcnt(0)
	v_writelane_b32 v241, s0, 18
	s_nop 1
	v_writelane_b32 v241, s1, 19
	s_add_u32 s0, s8, 0x148
	s_addc_u32 s1, s9, 0
	v_writelane_b32 v241, s0, 34
	s_nop 1
	v_writelane_b32 v241, s1, 35
	v_readlane_b32 s0, v243, 0
	s_cmpk_gt_i32 s0, 0xff
	v_readlane_b32 s1, v243, 1
	s_cbranch_scc1 .LBB0_1482
	v_readlane_b32 s0, v243, 7
	v_readlane_b32 s1, v243, 8
	v_readlane_b32 s4, v243, 0
	v_readlane_b32 s6, v243, 12
	s_load_dwordx2 s[2:3], s[0:1], 0x130
	s_lshr_b32 s7, s6, 2
	s_and_b32 s8, s6, 3
	s_bfe_u32 s11, s4, 0x20003
	s_lshr_b32 s50, s4, 5
	s_lshl_b32 s50, s50, 3
	s_and_b32 s51, s4, 7
	s_or_b32 s50, s50, s51
	s_lshr_b32 s9, s50, 2
	s_and_b32 s10, s50, 3
	v_and_b32_e32 v160, 15, v202
	v_lshrrev_b32_e32 v161, 4, v202
	v_lshlrev_b32_e32 v209, 2, v202
	s_lshl_b32 s50, s7, 15
	v_xor_b32_e32 v178, v161, v160
	v_lshlrev_b32_e32 v178, 4, v178
	v_lshl_add_u32 v162, v160, 9, v178
	v_add_u32_e32 v162, s50, v162
	s_lshl_b32 s51, s11, 6
	s_lshl_b32 s52, s8, 4
	s_add_i32 s51, s51, s52
	v_add_u32_e32 v179, s51, v160
	v_lshrrev_b32_e32 v180, 3, v179
	v_and_b32_e32 v181, 7, v179
	v_lshlrev_b32_e32 v181, 1, v181
	v_lshlrev_b32_e32 v182, 2, v161
	v_add_u32_e32 v183, 0, v182
	v_xor_b32_e32 v184, v180, v183
	v_lshlrev_b32_e32 v184, 4, v184
	v_lshl_add_u32 v184, v183, 9, v184
	v_add3_u32 v165, v184, v181, s50
	v_add_u32_e32 v183, 1, v182
	v_xor_b32_e32 v184, v180, v183
	v_lshlrev_b32_e32 v184, 4, v184
	v_lshl_add_u32 v184, v183, 9, v184
	v_add3_u32 v166, v184, v181, s50
	v_add_u32_e32 v183, 2, v182
	v_xor_b32_e32 v184, v180, v183
	v_lshlrev_b32_e32 v184, 4, v184
	v_lshl_add_u32 v184, v183, 9, v184
	v_add3_u32 v167, v184, v181, s50
	v_add_u32_e32 v183, 3, v182
	v_xor_b32_e32 v184, v180, v183
	v_lshlrev_b32_e32 v184, 4, v184
	v_lshl_add_u32 v184, v183, 9, v184
	v_add3_u32 v168, v184, v181, s50
	v_lshrrev_b32_e32 v185, 5, v202
	v_and_b32_e32 v186, 31, v202
	s_lshl_b32 s51, s6, 4
	v_add_u32_e32 v187, 0, v185
	v_xor_b32_e32 v188, v186, v187
	v_lshlrev_b32_e32 v188, 4, v188
	v_add_u32_e32 v187, s51, v187
	v_lshl_add_u32 v211, v187, 11, v188
	v_add_u32_e32 v187, 2, v185
	v_xor_b32_e32 v188, v186, v187
	v_lshlrev_b32_e32 v188, 4, v188
	v_add_u32_e32 v187, s51, v187
	v_lshl_add_u32 v212, v187, 11, v188
	v_add_u32_e32 v187, 4, v185
	v_xor_b32_e32 v188, v186, v187
	v_lshlrev_b32_e32 v188, 4, v188
	v_add_u32_e32 v187, s51, v187
	v_lshl_add_u32 v213, v187, 11, v188
	v_add_u32_e32 v187, 6, v185
	v_xor_b32_e32 v188, v186, v187
	v_lshlrev_b32_e32 v188, 4, v188
	v_add_u32_e32 v187, s51, v187
	v_lshl_add_u32 v214, v187, 11, v188
	v_add_u32_e32 v187, 8, v185
	v_xor_b32_e32 v188, v186, v187
	v_lshlrev_b32_e32 v188, 4, v188
	v_add_u32_e32 v187, s51, v187
	v_lshl_add_u32 v215, v187, 11, v188
	v_add_u32_e32 v187, 10, v185
	v_xor_b32_e32 v188, v186, v187
	v_lshlrev_b32_e32 v188, 4, v188
	v_add_u32_e32 v187, s51, v187
	v_lshl_add_u32 v216, v187, 11, v188
	v_add_u32_e32 v187, 12, v185
	v_xor_b32_e32 v188, v186, v187
	v_lshlrev_b32_e32 v188, 4, v188
	v_add_u32_e32 v187, s51, v187
	v_lshl_add_u32 v217, v187, 11, v188
	v_add_u32_e32 v187, 14, v185
	v_xor_b32_e32 v188, v186, v187
	v_lshlrev_b32_e32 v188, 4, v188
	v_add_u32_e32 v187, s51, v187
	v_lshl_add_u32 v218, v187, 11, v188
	s_lshl_b32 s51, s6, 7
	s_add_i32 s51, s51, 0x20000
	v_lshl_add_u32 v207, v160, 3, s51
	s_lshl_b32 s51, s8, 7
	s_add_i32 s51, s51, 0x20000
	v_lshl_add_u32 v208, v160, 3, s51
	s_lshl_b32 s51, s7, 6
	v_add_u32_e32 v189, s51, v182
	s_lshl_b32 s51, s8, 4
	v_add_u32_e32 v190, s51, v160
	v_lshlrev_b32_e32 v190, 1, v190
	v_lshl_add_u32 v210, v189, 11, v190
	s_waitcnt lgkmcnt(0)
	s_lshl_b32 s50, s10, 9
	s_add_u32 s16, s2, s50
	s_addc_u32 s17, s3, 0
	s_add_u32 s16, s16, 0x1b900000
	s_addc_u32 s17, s17, 0
	s_lshl_b32 s50, s10, 9
	s_lshl_b32 s51, s11, 7
	s_add_i32 s50, s50, s51
	s_add_u32 s18, s2, s50
	s_addc_u32 s19, s3, 0
	s_add_u32 s18, s18, 0x13100000
	s_addc_u32 s19, s19, 0
	s_add_u32 s20, s2, s50
	s_addc_u32 s21, s3, 0
	s_add_u32 s20, s20, 0x29100000
	s_addc_u32 s21, s21, 0
	s_lshl_b32 s50, s4, 18
	s_add_u32 s22, s2, s50
	s_addc_u32 s23, s3, 0
	s_add_u32 s22, s22, 0x20100000
	s_addc_u32 s23, s23, 0
	s_lshl_b32 s50, s10, 10
	s_lshl_b32 s51, s11, 6
	s_add_i32 s50, s50, s51
	s_lshl_b32 s51, s8, 4
	s_add_i32 s50, s50, s51
	s_add_i32 s50, s50, 0
	s_lshl_b32 s50, s50, 9
	s_add_u32 s46, s2, s50
	s_addc_u32 s47, s3, 0
	s_add_u32 s46, s46, 0x1000000
	s_addc_u32 s47, s47, 0
	s_add_u32 s48, s46, 0x20000
	s_addc_u32 s49, s47, 0
	v_lshlrev_b32_e32 v178, 9, v160
	v_lshl_add_u32 v178, v161, 4, v178
	global_load_dwordx4 v[0:3], v178, s[46:47]
	global_load_dwordx4 v[4:7], v178, s[46:47] offset:64
	global_load_dwordx4 v[8:11], v178, s[46:47] offset:128
	global_load_dwordx4 v[12:15], v178, s[46:47] offset:192
	global_load_dwordx4 v[16:19], v178, s[46:47] offset:256
	global_load_dwordx4 v[20:23], v178, s[46:47] offset:320
	global_load_dwordx4 v[24:27], v178, s[46:47] offset:384
	global_load_dwordx4 v[28:31], v178, s[46:47] offset:448
	global_load_dwordx4 v[32:35], v178, s[48:49]
	global_load_dwordx4 v[36:39], v178, s[48:49] offset:64
	global_load_dwordx4 v[40:43], v178, s[48:49] offset:128
	global_load_dwordx4 v[44:47], v178, s[48:49] offset:192
	global_load_dwordx4 v[48:51], v178, s[48:49] offset:256
	global_load_dwordx4 v[52:55], v178, s[48:49] offset:320
	global_load_dwordx4 v[56:59], v178, s[48:49] offset:384
	global_load_dwordx4 v[60:63], v178, s[48:49] offset:448
	s_load_dwordx2 s[46:47], s[0:1], 0xa0
	s_load_dwordx2 s[48:49], s[0:1], 0xb0
	s_load_dwordx2 s[40:41], s[0:1], 0xb8
	s_lshl_b32 s50, s10, 8
	s_lshl_b32 s51, s11, 6
	s_add_i32 s50, s50, s51
	s_lshl_b32 s51, s8, 4
	s_add_i32 s50, s50, s51
	v_add_u32_e32 v179, s50, v160
	v_lshlrev_b32_e32 v179, 2, v179
	s_waitcnt lgkmcnt(0)
	global_load_dword v173, v179, s[46:47]
	global_load_dword v174, v179, s[48:49]
	global_load_dword v175, v179, s[40:41]
	v_cmp_le_u32_e64 s[34:35], 16, v202
	v_cmp_le_u32_e64 s[36:37], 32, v202
	v_add_u32_e32 v204, -16, v202
	v_add_u32_e32 v205, -32, v202
	v_add_u32_e32 v206, 48, v160
	s_cmp_eq_u32 s7, 1
	s_cselect_b64 s[38:39], -1, 0
	v_and_b32_e32 v204, 63, v204
	v_lshlrev_b32_e32 v204, 2, v204
	v_and_b32_e32 v205, 63, v205
	v_lshlrev_b32_e32 v205, 2, v205
	v_and_b32_e32 v206, 63, v206
	v_lshlrev_b32_e32 v206, 2, v206
	v_mov_b32_e32 v176, 0
	s_mov_b32 s53, 0xbfb8aa3b
	s_mov_b32 s13, 0
	s_barrier
	s_cmp_lt_u32 s13, 2
	s_lshl_b32 s50, s13, 7
	s_lshl_b32 s51, s9, 8
	s_add_i32 s51, s51, 0x8000
	s_add_i32 s51, s51, s50
	s_lshl_b32 s59, s9, 11
	s_add_i32 s59, s59, s50
	s_addk_i32 s59, 0xff00
	s_cmp_lt_u32 s13, 2
	s_cselect_b32 s59, s51, s59
	s_lshl_b32 s52, s59, 11
	s_add_u32 s46, s16, s52
	s_addc_u32 s47, s17, 0
	s_lshl_b32 s52, s6, 13
	s_mov_b32 m0, s52
	s_add_i32 s52, s52, 0x400
	global_load_lds_dwordx4 v211, s[46:47]
	s_mov_b32 m0, s52
	s_add_i32 s52, s52, 0x400
	global_load_lds_dwordx4 v212, s[46:47]
	s_mov_b32 m0, s52
	s_add_i32 s52, s52, 0x400
	global_load_lds_dwordx4 v213, s[46:47]
	s_mov_b32 m0, s52
	s_add_i32 s52, s52, 0x400
	global_load_lds_dwordx4 v214, s[46:47]
	s_mov_b32 m0, s52
	s_add_i32 s52, s52, 0x400
	global_load_lds_dwordx4 v215, s[46:47]
	s_mov_b32 m0, s52
	s_add_i32 s52, s52, 0x400
	global_load_lds_dwordx4 v216, s[46:47]
	s_mov_b32 m0, s52
	s_add_i32 s52, s52, 0x400
	global_load_lds_dwordx4 v217, s[46:47]
	s_mov_b32 m0, s52
	s_nop 0
	global_load_lds_dwordx4 v218, s[46:47]
	s_waitcnt vmcnt(8)
	v_mul_f32_e32 v173, s53, v173
	v_mul_f32_e32 v174, s53, v174
	v_mul_f32_e32 v175, s53, v175
	v_exp_f32_e32 v175, v175
	s_nop 0
	v_add_f32_e32 v180, 1.0, v175
	v_log_f32_e32 v180, v180
	v_mov_b32_e32 v181, 0x3eaaaaab
	v_fma_f32 v181, v175, v181, -0.5
	v_fma_f32 v181, v175, v181, 1.0
	v_mul_f32_e32 v181, v175, v181
	v_mul_f32_e32 v181, 0x3fb8aa3b, v181
	v_cmp_gt_f32_e32 vcc, 0x3cf5c28f, v175
	s_nop 1
	v_cndmask_b32_e32 v175, v180, v181, vcc
	v_mul_f32_e32 v175, 0xc1000000, v175
	s_waitcnt vmcnt(0)
	s_barrier
	s_cmp_eq_u32 s13, 17
	s_cbranch_scc1 .Lmylru_nodma_1
	s_add_i32 s58, s13, 1
	s_cmp_lt_u32 s58, 2
	s_lshl_b32 s50, s58, 7
	s_lshl_b32 s51, s9, 8
	s_add_i32 s51, s51, 0x8000
	s_add_i32 s51, s51, s50
	s_lshl_b32 s59, s9, 11
	s_add_i32 s59, s59, s50
	s_addk_i32 s59, 0xff00
	s_cmp_lt_u32 s58, 2
	s_cselect_b32 s59, s51, s59
	s_lshl_b32 s52, s59, 11
	s_add_u32 s46, s16, s52
	s_addc_u32 s47, s17, 0
	s_lshl_b32 s52, s6, 13
	s_add_i32 s52, s52, 0x10000
	s_mov_b32 m0, s52
	s_add_i32 s52, s52, 0x400
	global_load_lds_dwordx4 v211, s[46:47]
	s_mov_b32 m0, s52
	s_add_i32 s52, s52, 0x400
	global_load_lds_dwordx4 v212, s[46:47]
	s_mov_b32 m0, s52
	s_add_i32 s52, s52, 0x400
	global_load_lds_dwordx4 v213, s[46:47]
	s_mov_b32 m0, s52
	s_add_i32 s52, s52, 0x400
	global_load_lds_dwordx4 v214, s[46:47]
	s_mov_b32 m0, s52
	s_add_i32 s52, s52, 0x400
	global_load_lds_dwordx4 v215, s[46:47]
	s_mov_b32 m0, s52
	s_add_i32 s52, s52, 0x400
	global_load_lds_dwordx4 v216, s[46:47]
	s_mov_b32 m0, s52
	s_add_i32 s52, s52, 0x400
	global_load_lds_dwordx4 v217, s[46:47]
	s_mov_b32 m0, s52
	s_nop 0
	global_load_lds_dwordx4 v218, s[46:47]

.Lmylru_nodma_4:
	v_or_b32_e32 v163, 0x10000, v162
	ds_read_b128 v[96:99], v163
	ds_read_b128 v[100:103], v163 offset:8192
	ds_read_b128 v[104:107], v163 offset:16384
	ds_read_b128 v[108:111], v163 offset:24576
	v_xor_b32_e32 v164, 0x40, v163
	ds_read_b128 v[112:115], v164
	ds_read_b128 v[116:119], v164 offset:8192
	ds_read_b128 v[120:123], v164 offset:16384
	ds_read_b128 v[124:127], v164 offset:24576
	s_waitcnt lgkmcnt(7)
	v_mfma_f32_16x16x32_bf16 v[64:67], v[96:99], v[0:3], 0
	v_mfma_f32_16x16x32_bf16 v[68:71], v[96:99], v[32:35], 0
	v_xor_b32_e32 v164, 0x80, v163
	ds_read_b128 v[96:99], v164
	s_waitcnt lgkmcnt(7)
	v_mfma_f32_16x16x32_bf16 v[72:75], v[100:103], v[0:3], 0
	v_mfma_f32_16x16x32_bf16 v[76:79], v[100:103], v[32:35], 0
	ds_read_b128 v[100:103], v164 offset:8192
	s_waitcnt lgkmcnt(7)
	v_mfma_f32_16x16x32_bf16 v[80:83], v[104:107], v[0:3], 0
	v_mfma_f32_16x16x32_bf16 v[84:87], v[104:107], v[32:35], 0
	ds_read_b128 v[104:107], v164 offset:16384
	s_waitcnt lgkmcnt(7)
	v_mfma_f32_16x16x32_bf16 v[88:91], v[108:111], v[0:3], 0
	v_mfma_f32_16x16x32_bf16 v[92:95], v[108:111], v[32:35], 0
	ds_read_b128 v[108:111], v164 offset:24576
	s_waitcnt lgkmcnt(7)
	v_mfma_f32_16x16x32_bf16 v[64:67], v[112:115], v[4:7], v[64:67]
	v_mfma_f32_16x16x32_bf16 v[68:71], v[112:115], v[36:39], v[68:71]
	v_xor_b32_e32 v164, 0xc0, v163
	ds_read_b128 v[112:115], v164
	s_waitcnt lgkmcnt(7)
	v_mfma_f32_16x16x32_bf16 v[72:75], v[116:119], v[4:7], v[72:75]
	v_mfma_f32_16x16x32_bf16 v[76:79], v[116:119], v[36:39], v[76:79]
	ds_read_b128 v[116:119], v164 offset:8192
	s_waitcnt lgkmcnt(7)
	v_mfma_f32_16x16x32_bf16 v[80:83], v[120:123], v[4:7], v[80:83]
	v_mfma_f32_16x16x32_bf16 v[84:87], v[120:123], v[36:39], v[84:87]
	ds_read_b128 v[120:123], v164 offset:16384
	s_waitcnt lgkmcnt(7)
	v_mfma_f32_16x16x32_bf16 v[88:91], v[124:127], v[4:7], v[88:91]
	v_mfma_f32_16x16x32_bf16 v[92:95], v[124:127], v[36:39], v[92:95]
	ds_read_b128 v[124:127], v164 offset:24576
	s_waitcnt lgkmcnt(7)
	v_mfma_f32_16x16x32_bf16 v[64:67], v[96:99], v[8:11], v[64:67]
	v_mfma_f32_16x16x32_bf16 v[68:71], v[96:99], v[40:43], v[68:71]
	v_xor_b32_e32 v164, 0x100, v163
	ds_read_b128 v[96:99], v164
	s_waitcnt lgkmcnt(7)
	v_mfma_f32_16x16x32_bf16 v[72:75], v[100:103], v[8:11], v[72:75]
	v_mfma_f32_16x16x32_bf16 v[76:79], v[100:103], v[40:43], v[76:79]
	ds_read_b128 v[100:103], v164 offset:8192
	s_waitcnt lgkmcnt(7)
	v_mfma_f32_16x16x32_bf16 v[80:83], v[104:107], v[8:11], v[80:83]
	v_mfma_f32_16x16x32_bf16 v[84:87], v[104:107], v[40:43], v[84:87]
	ds_read_b128 v[104:107], v164 offset:16384
	s_waitcnt lgkmcnt(7)
	v_mfma_f32_16x16x32_bf16 v[88:91], v[108:111], v[8:11], v[88:91]
	v_mfma_f32_16x16x32_bf16 v[92:95], v[108:111], v[40:43], v[92:95]
	ds_read_b128 v[108:111], v164 offset:24576
	s_waitcnt lgkmcnt(7)
	v_mfma_f32_16x16x32_bf16 v[64:67], v[112:115], v[12:15], v[64:67]
	v_mfma_f32_16x16x32_bf16 v[68:71], v[112:115], v[44:47], v[68:71]
	v_xor_b32_e32 v164, 0x140, v163
	ds_read_b128 v[112:115], v164
	s_waitcnt lgkmcnt(7)
	v_mfma_f32_16x16x32_bf16 v[72:75], v[116:119], v[12:15], v[72:75]
	v_mfma_f32_16x16x32_bf16 v[76:79], v[116:119], v[44:47], v[76:79]
	ds_read_b128 v[116:119], v164 offset:8192
	s_waitcnt lgkmcnt(7)
	v_mfma_f32_16x16x32_bf16 v[80:83], v[120:123], v[12:15], v[80:83]
	v_mfma_f32_16x16x32_bf16 v[84:87], v[120:123], v[44:47], v[84:87]
	ds_read_b128 v[120:123], v164 offset:16384
	s_waitcnt lgkmcnt(7)
	v_mfma_f32_16x16x32_bf16 v[88:91], v[124:127], v[12:15], v[88:91]
	v_mfma_f32_16x16x32_bf16 v[92:95], v[124:127], v[44:47], v[92:95]
	ds_read_b128 v[124:127], v164 offset:24576
	s_waitcnt lgkmcnt(7)
	v_mfma_f32_16x16x32_bf16 v[64:67], v[96:99], v[16:19], v[64:67]
	v_mfma_f32_16x16x32_bf16 v[68:71], v[96:99], v[48:51], v[68:71]
	v_xor_b32_e32 v164, 0x180, v163
	ds_read_b128 v[96:99], v164
	s_waitcnt lgkmcnt(7)
	v_mfma_f32_16x16x32_bf16 v[72:75], v[100:103], v[16:19], v[72:75]
	v_mfma_f32_16x16x32_bf16 v[76:79], v[100:103], v[48:51], v[76:79]
	ds_read_b128 v[100:103], v164 offset:8192
	s_waitcnt lgkmcnt(7)
	v_mfma_f32_16x16x32_bf16 v[80:83], v[104:107], v[16:19], v[80:83]
	v_mfma_f32_16x16x32_bf16 v[84:87], v[104:107], v[48:51], v[84:87]
	ds_read_b128 v[104:107], v164 offset:16384
	s_waitcnt lgkmcnt(7)
	v_mfma_f32_16x16x32_bf16 v[88:91], v[108:111], v[16:19], v[88:91]
	v_mfma_f32_16x16x32_bf16 v[92:95], v[108:111], v[48:51], v[92:95]
	ds_read_b128 v[108:111], v164 offset:24576
	s_waitcnt lgkmcnt(7)
	v_mfma_f32_16x16x32_bf16 v[64:67], v[112:115], v[20:23], v[64:67]
	v_mfma_f32_16x16x32_bf16 v[68:71], v[112:115], v[52:55], v[68:71]
	v_xor_b32_e32 v164, 0x1c0, v163
	ds_read_b128 v[112:115], v164
	s_waitcnt lgkmcnt(7)
	v_mfma_f32_16x16x32_bf16 v[72:75], v[116:119], v[20:23], v[72:75]
	v_mfma_f32_16x16x32_bf16 v[76:79], v[116:119], v[52:55], v[76:79]
	ds_read_b128 v[116:119], v164 offset:8192
	s_waitcnt lgkmcnt(7)
	v_mfma_f32_16x16x32_bf16 v[80:83], v[120:123], v[20:23], v[80:83]
	v_mfma_f32_16x16x32_bf16 v[84:87], v[120:123], v[52:55], v[84:87]
	ds_read_b128 v[120:123], v164 offset:16384
	s_waitcnt lgkmcnt(7)
	v_mfma_f32_16x16x32_bf16 v[88:91], v[124:127], v[20:23], v[88:91]
	v_mfma_f32_16x16x32_bf16 v[92:95], v[124:127], v[52:55], v[92:95]
	ds_read_b128 v[124:127], v164 offset:24576
	s_waitcnt lgkmcnt(7)
	v_mfma_f32_16x16x32_bf16 v[64:67], v[96:99], v[24:27], v[64:67]
	v_mfma_f32_16x16x32_bf16 v[68:71], v[96:99], v[56:59], v[68:71]
	s_waitcnt lgkmcnt(6)
	v_mfma_f32_16x16x32_bf16 v[72:75], v[100:103], v[24:27], v[72:75]
	v_mfma_f32_16x16x32_bf16 v[76:79], v[100:103], v[56:59], v[76:79]
	s_waitcnt lgkmcnt(5)
	v_mfma_f32_16x16x32_bf16 v[80:83], v[104:107], v[24:27], v[80:83]
	v_mfma_f32_16x16x32_bf16 v[84:87], v[104:107], v[56:59], v[84:87]
	s_waitcnt lgkmcnt(4)
	v_mfma_f32_16x16x32_bf16 v[88:91], v[108:111], v[24:27], v[88:91]
	v_mfma_f32_16x16x32_bf16 v[92:95], v[108:111], v[56:59], v[92:95]
	s_waitcnt lgkmcnt(3)
	v_mfma_f32_16x16x32_bf16 v[64:67], v[112:115], v[28:31], v[64:67]
	v_mfma_f32_16x16x32_bf16 v[68:71], v[112:115], v[60:63], v[68:71]
	s_waitcnt lgkmcnt(2)
	v_mfma_f32_16x16x32_bf16 v[72:75], v[116:119], v[28:31], v[72:75]
	v_mfma_f32_16x16x32_bf16 v[76:79], v[116:119], v[60:63], v[76:79]
	s_waitcnt lgkmcnt(1)
	v_mfma_f32_16x16x32_bf16 v[80:83], v[120:123], v[28:31], v[80:83]
	v_mfma_f32_16x16x32_bf16 v[84:87], v[120:123], v[60:63], v[84:87]
	s_waitcnt lgkmcnt(0)
	v_mfma_f32_16x16x32_bf16 v[88:91], v[124:127], v[28:31], v[88:91]
	v_mfma_f32_16x16x32_bf16 v[92:95], v[124:127], v[60:63], v[92:95]
	v_or_b32_e32 v169, 0x10000, v165
	v_or_b32_e32 v170, 0x10000, v166
	v_or_b32_e32 v171, 0x10000, v167
	v_or_b32_e32 v172, 0x10000, v168
	ds_read_u16 v144, v169
	ds_read_u16 v145, v170
	ds_read_u16 v146, v171
	ds_read_u16 v147, v172
	ds_read_u16 v148, v169 offset:8192
	ds_read_u16 v149, v170 offset:8192
	ds_read_u16 v150, v171 offset:8192
	ds_read_u16 v151, v172 offset:8192
	ds_read_u16 v152, v169 offset:16384
	ds_read_u16 v153, v170 offset:16384
	ds_read_u16 v154, v171 offset:16384
	ds_read_u16 v155, v172 offset:16384
	ds_read_u16 v156, v169 offset:24576
	ds_read_u16 v157, v170 offset:24576
	ds_read_u16 v158, v171 offset:24576
	ds_read_u16 v159, v172 offset:24576
	s_nop 7
	v_fma_f32 v178, v64, s53, v173
	v_fma_f32 v179, v65, s53, v173
	v_fma_f32 v180, v66, s53, v173
	v_fma_f32 v181, v67, s53, v173
	v_fma_f32 v182, v72, s53, v173
	v_fma_f32 v183, v73, s53, v173
	v_fma_f32 v184, v74, s53, v173
	v_fma_f32 v185, v75, s53, v173
	v_fma_f32 v186, v68, s53, v174
	v_fma_f32 v187, v69, s53, v174
	v_fma_f32 v188, v70, s53, v174
	v_fma_f32 v189, v71, s53, v174
	v_fma_f32 v190, v76, s53, v174
	v_fma_f32 v191, v77, s53, v174
	v_fma_f32 v192, v78, s53, v174
	v_fma_f32 v193, v79, s53, v174
	v_exp_f32_e32 v178, v178
	v_exp_f32_e32 v179, v179
	v_exp_f32_e32 v180, v180
	v_exp_f32_e32 v181, v181
	v_exp_f32_e32 v182, v182
	v_exp_f32_e32 v183, v183
	v_exp_f32_e32 v184, v184
	v_exp_f32_e32 v185, v185
	v_exp_f32_e32 v186, v186
	v_exp_f32_e32 v187, v187
	v_exp_f32_e32 v188, v188
	v_exp_f32_e32 v189, v189
	v_exp_f32_e32 v190, v190
	v_exp_f32_e32 v191, v191
	v_exp_f32_e32 v192, v192
	v_exp_f32_e32 v193, v193
	v_add_f32_e32 v178, 1.0, v178
	v_add_f32_e32 v179, 1.0, v179
	v_add_f32_e32 v180, 1.0, v180
	v_add_f32_e32 v181, 1.0, v181
	v_add_f32_e32 v182, 1.0, v182
	v_add_f32_e32 v183, 1.0, v183
	v_add_f32_e32 v184, 1.0, v184
	v_add_f32_e32 v185, 1.0, v185
	v_add_f32_e32 v186, 1.0, v186
	v_add_f32_e32 v187, 1.0, v187
	v_add_f32_e32 v188, 1.0, v188
	v_add_f32_e32 v189, 1.0, v189
	v_add_f32_e32 v190, 1.0, v190
	v_add_f32_e32 v191, 1.0, v191
	v_add_f32_e32 v192, 1.0, v192
	v_add_f32_e32 v193, 1.0, v193
	v_rcp_f32_e32 v178, v178
	v_rcp_f32_e32 v179, v179
	v_rcp_f32_e32 v180, v180
	v_rcp_f32_e32 v181, v181
	v_rcp_f32_e32 v182, v182
	v_rcp_f32_e32 v183, v183
	v_rcp_f32_e32 v184, v184
	v_rcp_f32_e32 v185, v185
	v_rcp_f32_e32 v186, v186
	v_rcp_f32_e32 v187, v187
	v_rcp_f32_e32 v188, v188
	v_rcp_f32_e32 v189, v189
	v_rcp_f32_e32 v190, v190
	v_rcp_f32_e32 v191, v191
	v_rcp_f32_e32 v192, v192
	v_rcp_f32_e32 v193, v193
	v_mul_f32_e32 v178, v175, v178
	v_mul_f32_e32 v179, v175, v179
	v_mul_f32_e32 v180, v175, v180
	v_mul_f32_e32 v181, v175, v181
	v_mul_f32_e32 v182, v175, v182
	v_mul_f32_e32 v183, v175, v183
	v_mul_f32_e32 v184, v175, v184
	v_mul_f32_e32 v185, v175, v185
	v_exp_f32_e32 v96, v178
	v_exp_f32_e32 v97, v179
	v_exp_f32_e32 v98, v180
	v_exp_f32_e32 v99, v181
	v_exp_f32_e32 v100, v182
	v_exp_f32_e32 v101, v183
	v_exp_f32_e32 v102, v184
	v_exp_f32_e32 v103, v185
	s_nop 0
	v_fma_f32 v194, -v96, v96, 1.0
	v_fma_f32 v195, -v97, v97, 1.0
	v_fma_f32 v196, -v98, v98, 1.0
	v_fma_f32 v197, -v99, v99, 1.0
	v_fma_f32 v198, -v100, v100, 1.0
	v_fma_f32 v199, -v101, v101, 1.0
	v_fma_f32 v200, -v102, v102, 1.0
	v_fma_f32 v201, -v103, v103, 1.0
	v_max_f32_e32 v194, 0, v194
	v_max_f32_e32 v195, 0, v195
	v_max_f32_e32 v196, 0, v196
	v_max_f32_e32 v197, 0, v197
	v_max_f32_e32 v198, 0, v198
	v_max_f32_e32 v199, 0, v199
	v_max_f32_e32 v200, 0, v200
	v_max_f32_e32 v201, 0, v201
	v_sqrt_f32_e32 v194, v194
	v_sqrt_f32_e32 v195, v195
	v_sqrt_f32_e32 v196, v196
	v_sqrt_f32_e32 v197, v197
	v_sqrt_f32_e32 v198, v198
	v_sqrt_f32_e32 v199, v199
	v_sqrt_f32_e32 v200, v200
	v_sqrt_f32_e32 v201, v201
	s_waitcnt lgkmcnt(8)
	v_lshlrev_b32_e32 v144, 16, v144
	v_lshlrev_b32_e32 v145, 16, v145
	v_lshlrev_b32_e32 v146, 16, v146
	v_lshlrev_b32_e32 v147, 16, v147
	v_lshlrev_b32_e32 v148, 16, v148
	v_lshlrev_b32_e32 v149, 16, v149
	v_lshlrev_b32_e32 v150, 16, v150
	v_lshlrev_b32_e32 v151, 16, v151
	v_mul_f32_e32 v194, v194, v186
	v_mul_f32_e32 v195, v195, v187
	v_mul_f32_e32 v196, v196, v188
	v_mul_f32_e32 v197, v197, v189
	v_mul_f32_e32 v198, v198, v190
	v_mul_f32_e32 v199, v199, v191
	v_mul_f32_e32 v200, v200, v192
	v_mul_f32_e32 v201, v201, v193
	v_mul_f32_e32 v144, v194, v144
	v_mul_f32_e32 v145, v195, v145
	v_mul_f32_e32 v146, v196, v146
	v_mul_f32_e32 v147, v197, v147
	v_mul_f32_e32 v148, v198, v148
	v_mul_f32_e32 v149, v199, v149
	v_mul_f32_e32 v150, v200, v150
	v_mul_f32_e32 v151, v201, v151
	v_fma_f32 v178, v80, s53, v173
	v_fma_f32 v179, v81, s53, v173
	v_fma_f32 v180, v82, s53, v173
	v_fma_f32 v181, v83, s53, v173
	v_fma_f32 v182, v88, s53, v173
	v_fma_f32 v183, v89, s53, v173
	v_fma_f32 v184, v90, s53, v173
	v_fma_f32 v185, v91, s53, v173
	v_fma_f32 v186, v84, s53, v174
	v_fma_f32 v187, v85, s53, v174
	v_fma_f32 v188, v86, s53, v174
	v_fma_f32 v189, v87, s53, v174
	v_fma_f32 v190, v92, s53, v174
	v_fma_f32 v191, v93, s53, v174
	v_fma_f32 v192, v94, s53, v174
	v_fma_f32 v193, v95, s53, v174
	v_exp_f32_e32 v178, v178
	v_exp_f32_e32 v179, v179
	v_exp_f32_e32 v180, v180
	v_exp_f32_e32 v181, v181
	v_exp_f32_e32 v182, v182
	v_exp_f32_e32 v183, v183
	v_exp_f32_e32 v184, v184
	v_exp_f32_e32 v185, v185
	v_exp_f32_e32 v186, v186
	v_exp_f32_e32 v187, v187
	v_exp_f32_e32 v188, v188
	v_exp_f32_e32 v189, v189
	v_exp_f32_e32 v190, v190
	v_exp_f32_e32 v191, v191
	v_exp_f32_e32 v192, v192
	v_exp_f32_e32 v193, v193
	v_add_f32_e32 v178, 1.0, v178
	v_add_f32_e32 v179, 1.0, v179
	v_add_f32_e32 v180, 1.0, v180
	v_add_f32_e32 v181, 1.0, v181
	v_add_f32_e32 v182, 1.0, v182
	v_add_f32_e32 v183, 1.0, v183
	v_add_f32_e32 v184, 1.0, v184
	v_add_f32_e32 v185, 1.0, v185
	v_add_f32_e32 v186, 1.0, v186
	v_add_f32_e32 v187, 1.0, v187
	v_add_f32_e32 v188, 1.0, v188
	v_add_f32_e32 v189, 1.0, v189
	v_add_f32_e32 v190, 1.0, v190
	v_add_f32_e32 v191, 1.0, v191
	v_add_f32_e32 v192, 1.0, v192
	v_add_f32_e32 v193, 1.0, v193
	v_rcp_f32_e32 v178, v178
	v_rcp_f32_e32 v179, v179
	v_rcp_f32_e32 v180, v180
	v_rcp_f32_e32 v181, v181
	v_rcp_f32_e32 v182, v182
	v_rcp_f32_e32 v183, v183
	v_rcp_f32_e32 v184, v184
	v_rcp_f32_e32 v185, v185
	v_rcp_f32_e32 v186, v186
	v_rcp_f32_e32 v187, v187
	v_rcp_f32_e32 v188, v188
	v_rcp_f32_e32 v189, v189
	v_rcp_f32_e32 v190, v190
	v_rcp_f32_e32 v191, v191
	v_rcp_f32_e32 v192, v192
	v_rcp_f32_e32 v193, v193
	v_mul_f32_e32 v178, v175, v178
	v_mul_f32_e32 v179, v175, v179
	v_mul_f32_e32 v180, v175, v180
	v_mul_f32_e32 v181, v175, v181
	v_mul_f32_e32 v182, v175, v182
	v_mul_f32_e32 v183, v175, v183
	v_mul_f32_e32 v184, v175, v184
	v_mul_f32_e32 v185, v175, v185
	v_exp_f32_e32 v104, v178
	v_exp_f32_e32 v105, v179
	v_exp_f32_e32 v106, v180
	v_exp_f32_e32 v107, v181
	v_exp_f32_e32 v108, v182
	v_exp_f32_e32 v109, v183
	v_exp_f32_e32 v110, v184
	v_exp_f32_e32 v111, v185
	s_nop 0
	v_fma_f32 v194, -v104, v104, 1.0
	v_fma_f32 v195, -v105, v105, 1.0
	v_fma_f32 v196, -v106, v106, 1.0
	v_fma_f32 v197, -v107, v107, 1.0
	v_fma_f32 v198, -v108, v108, 1.0
	v_fma_f32 v199, -v109, v109, 1.0
	v_fma_f32 v200, -v110, v110, 1.0
	v_fma_f32 v201, -v111, v111, 1.0
	v_max_f32_e32 v194, 0, v194
	v_max_f32_e32 v195, 0, v195
	v_max_f32_e32 v196, 0, v196
	v_max_f32_e32 v197, 0, v197
	v_max_f32_e32 v198, 0, v198
	v_max_f32_e32 v199, 0, v199
	v_max_f32_e32 v200, 0, v200
	v_max_f32_e32 v201, 0, v201
	v_sqrt_f32_e32 v194, v194
	v_sqrt_f32_e32 v195, v195
	v_sqrt_f32_e32 v196, v196
	v_sqrt_f32_e32 v197, v197
	v_sqrt_f32_e32 v198, v198
	v_sqrt_f32_e32 v199, v199
	v_sqrt_f32_e32 v200, v200
	v_sqrt_f32_e32 v201, v201
	s_waitcnt lgkmcnt(0)
	v_lshlrev_b32_e32 v152, 16, v152
	v_lshlrev_b32_e32 v153, 16, v153
	v_lshlrev_b32_e32 v154, 16, v154
	v_lshlrev_b32_e32 v155, 16, v155
	v_lshlrev_b32_e32 v156, 16, v156
	v_lshlrev_b32_e32 v157, 16, v157
	v_lshlrev_b32_e32 v158, 16, v158
	v_lshlrev_b32_e32 v159, 16, v159
	v_mul_f32_e32 v194, v194, v186
	v_mul_f32_e32 v195, v195, v187
	v_mul_f32_e32 v196, v196, v188
	v_mul_f32_e32 v197, v197, v189
	v_mul_f32_e32 v198, v198, v190
	v_mul_f32_e32 v199, v199, v191
	v_mul_f32_e32 v200, v200, v192
	v_mul_f32_e32 v201, v201, v193
	v_mul_f32_e32 v152, v194, v152
	v_mul_f32_e32 v153, v195, v153
	v_mul_f32_e32 v154, v196, v154
	v_mul_f32_e32 v155, v197, v155
	v_mul_f32_e32 v156, v198, v156
	v_mul_f32_e32 v157, v199, v157
	v_mul_f32_e32 v158, v200, v158
	v_mul_f32_e32 v159, v201, v159
	v_fma_f32 v145, v97, v144, v145
	v_fma_f32 v149, v101, v148, v149
	v_fma_f32 v153, v105, v152, v153
	v_fma_f32 v157, v109, v156, v157
	v_mul_f32_e32 v97, v97, v96
	v_mul_f32_e32 v101, v101, v100
	v_mul_f32_e32 v105, v105, v104
	v_mul_f32_e32 v109, v109, v108
	v_fma_f32 v146, v98, v145, v146
	v_fma_f32 v150, v102, v149, v150
	v_fma_f32 v154, v106, v153, v154
	v_fma_f32 v158, v110, v157, v158
	v_mul_f32_e32 v98, v98, v97
	v_mul_f32_e32 v102, v102, v101
	v_mul_f32_e32 v106, v106, v105
	v_mul_f32_e32 v110, v110, v109
	v_fma_f32 v147, v99, v146, v147
	v_fma_f32 v151, v103, v150, v151
	v_fma_f32 v155, v107, v154, v155
	v_fma_f32 v159, v111, v158, v159
	v_mul_f32_e32 v99, v99, v98
	v_mul_f32_e32 v103, v103, v102
	v_mul_f32_e32 v107, v107, v106
	v_mul_f32_e32 v111, v111, v110
	ds_bpermute_b32 v178, v204, v99
	ds_bpermute_b32 v182, v204, v147
	ds_bpermute_b32 v179, v204, v103
	ds_bpermute_b32 v183, v204, v151
	ds_bpermute_b32 v180, v204, v107
	ds_bpermute_b32 v184, v204, v155
	ds_bpermute_b32 v181, v204, v111
	ds_bpermute_b32 v185, v204, v159
	s_waitcnt lgkmcnt(0)
	v_fma_f32 v186, v182, v99, v147
	v_cndmask_b32_e64 v178, 1.0, v178, s[34:35]
	v_fma_f32 v187, v183, v103, v151
	v_cndmask_b32_e64 v179, 1.0, v179, s[34:35]
	v_fma_f32 v188, v184, v107, v155
	v_cndmask_b32_e64 v180, 1.0, v180, s[34:35]
	v_fma_f32 v189, v185, v111, v159
	v_cndmask_b32_e64 v181, 1.0, v181, s[34:35]
	v_cndmask_b32_e64 v223, v147, v186, s[34:35]
	v_mul_f32_e32 v219, v99, v178
	v_cndmask_b32_e64 v224, v151, v187, s[34:35]
	v_mul_f32_e32 v220, v103, v179
	v_cndmask_b32_e64 v225, v155, v188, s[34:35]
	v_mul_f32_e32 v221, v107, v180
	v_cndmask_b32_e64 v226, v159, v189, s[34:35]
	v_mul_f32_e32 v222, v111, v181
	ds_bpermute_b32 v178, v205, v219
	ds_bpermute_b32 v182, v205, v223
	ds_bpermute_b32 v179, v205, v220
	ds_bpermute_b32 v183, v205, v224
	ds_bpermute_b32 v180, v205, v221
	ds_bpermute_b32 v184, v205, v225
	ds_bpermute_b32 v181, v205, v222
	ds_bpermute_b32 v185, v205, v226
	s_waitcnt lgkmcnt(0)
	v_fma_f32 v186, v182, v219, v223
	v_cndmask_b32_e64 v178, 1.0, v178, s[36:37]
	v_fma_f32 v187, v183, v220, v224
	v_cndmask_b32_e64 v179, 1.0, v179, s[36:37]
	v_fma_f32 v188, v184, v221, v225
	v_cndmask_b32_e64 v180, 1.0, v180, s[36:37]
	v_fma_f32 v189, v185, v222, v226
	v_cndmask_b32_e64 v181, 1.0, v181, s[36:37]
	v_cndmask_b32_e64 v223, v223, v186, s[36:37]
	v_mul_f32_e32 v219, v219, v178
	v_cndmask_b32_e64 v224, v224, v187, s[36:37]
	v_mul_f32_e32 v220, v220, v179
	v_cndmask_b32_e64 v225, v225, v188, s[36:37]
	v_mul_f32_e32 v221, v221, v180
	v_cndmask_b32_e64 v226, v226, v189, s[36:37]
	v_mul_f32_e32 v222, v222, v181
	ds_bpermute_b32 v227, v204, v219
	ds_bpermute_b32 v231, v204, v223
	ds_bpermute_b32 v235, v206, v219
	ds_bpermute_b32 v239, v206, v223
	ds_bpermute_b32 v228, v204, v220
	ds_bpermute_b32 v232, v204, v224
	ds_bpermute_b32 v236, v206, v220
	ds_bpermute_b32 v244, v206, v224
	ds_bpermute_b32 v229, v204, v221
	ds_bpermute_b32 v233, v204, v225
	ds_bpermute_b32 v237, v206, v221
	ds_bpermute_b32 v245, v206, v225
	ds_bpermute_b32 v230, v204, v222
	ds_bpermute_b32 v234, v204, v226
	ds_bpermute_b32 v238, v206, v222
	ds_bpermute_b32 v246, v206, v226
	s_waitcnt lgkmcnt(0)
	v_cndmask_b32_e64 v227, 1.0, v227, s[34:35]
	v_cndmask_b32_e64 v231, 0, v231, s[34:35]
	v_cndmask_b32_e64 v228, 1.0, v228, s[34:35]
	v_cndmask_b32_e64 v232, 0, v232, s[34:35]
	v_cndmask_b32_e64 v229, 1.0, v229, s[34:35]
	v_cndmask_b32_e64 v233, 0, v233, s[34:35]
	v_cndmask_b32_e64 v230, 1.0, v230, s[34:35]
	v_cndmask_b32_e64 v234, 0, v234, s[34:35]
	v_mov_b32_e32 v190, v235
	v_mov_b32_e32 v194, v239
	v_mov_b32_e32 v198, v190
	v_mov_b32_e32 v201, v194
	v_fma_f32 v194, v194, v236, v244
	v_mul_f32_e32 v190, v190, v236
	v_mov_b32_e32 v199, v190
	v_mov_b32_e32 v177, v194
	v_fma_f32 v194, v194, v237, v245
	v_mul_f32_e32 v190, v190, v237
	v_mov_b32_e32 v200, v190
	v_mov_b32_e32 v203, v194
	v_fma_f32 v194, v194, v238, v246
	v_mul_f32_e32 v190, v190, v238
	v_mov_b32_e32 v191, v194
	ds_write_b64 v207, v[190:191] offset:1024
	s_waitcnt lgkmcnt(0)
	s_barrier
	ds_read_b64 v[178:179], v208 offset:1024
	ds_read_b64 v[180:181], v208 offset:1536
	s_waitcnt lgkmcnt(0)
	v_fma_f32 v182, v176, v178, v179
	v_cndmask_b32_e64 v183, v176, v182, s[38:39]
	v_fma_f32 v176, v182, v180, v181
	v_mov_b32_e32 v184, v183
	v_fma_f32 v185, v183, v198, v201
	v_fma_f32 v186, v183, v199, v177
	v_fma_f32 v187, v183, v200, v203
	v_fma_f32 v184, v184, v227, v231
	v_fma_f32 v185, v185, v228, v232
	v_fma_f32 v186, v186, v229, v233
	v_fma_f32 v187, v187, v230, v234
	v_fma_f32 v144, v184, v96, v144
	v_fma_f32 v148, v185, v100, v148
	v_fma_f32 v152, v186, v104, v152
	v_fma_f32 v156, v187, v108, v156
	v_fma_f32 v145, v184, v97, v145
	v_fma_f32 v149, v185, v101, v149
	v_fma_f32 v153, v186, v105, v153
	v_fma_f32 v157, v187, v109, v157
	v_fma_f32 v146, v184, v98, v146
	v_fma_f32 v150, v185, v102, v150
	v_fma_f32 v154, v186, v106, v154
	v_fma_f32 v158, v187, v110, v158
	v_fma_f32 v147, v184, v99, v147
	v_fma_f32 v151, v185, v103, v151
	v_fma_f32 v155, v186, v107, v155
	v_fma_f32 v159, v187, v111, v159
	v_cvt_pk_bf16_f32 v178, v144, v145
	v_cvt_pk_bf16_f32 v179, v146, v147
	v_cvt_pk_bf16_f32 v180, v148, v149
	v_cvt_pk_bf16_f32 v181, v150, v151
	v_cvt_pk_bf16_f32 v182, v152, v153
	v_cvt_pk_bf16_f32 v183, v154, v155
	v_cvt_pk_bf16_f32 v184, v156, v157
	v_cvt_pk_bf16_f32 v185, v158, v159
	global_store_dword v209, v178, s[44:45]
	global_store_dword v209, v179, s[44:45] offset:256
	global_store_dword v209, v180, s[44:45] offset:512
	global_store_dword v209, v181, s[44:45] offset:768
	global_store_dword v209, v182, s[44:45] offset:1024
	global_store_dword v209, v183, s[44:45] offset:1280
	global_store_dword v209, v184, s[44:45] offset:1536
	global_store_dword v209, v185, s[44:45] offset:1792
	s_add_i32 s13, s13, 1
	s_add_i32 s60, s60, -1
	s_cmp_lg_u32 s60, 0
	s_cbranch_scc1 .Lmylru_loop_0
	s_lshl_b32 s50, s10, 10
	s_lshl_b32 s51, s11, 6
	s_add_i32 s50, s50, s51
	s_lshl_b32 s51, s8, 4
	s_add_i32 s50, s50, s51
	s_add_i32 s50, s50, 512
	s_lshl_b32 s50, s50, 9
	s_add_u32 s46, s2, s50
	s_addc_u32 s47, s3, 0
	s_add_u32 s46, s46, 0x1000000
	s_addc_u32 s47, s47, 0
	s_add_u32 s48, s46, 0x20000
	s_addc_u32 s49, s47, 0
	v_lshlrev_b32_e32 v178, 9, v160
	v_lshl_add_u32 v178, v161, 4, v178
	global_load_dwordx4 v[0:3], v178, s[46:47]
	global_load_dwordx4 v[4:7], v178, s[46:47] offset:64
	global_load_dwordx4 v[8:11], v178, s[46:47] offset:128
	global_load_dwordx4 v[12:15], v178, s[46:47] offset:192
	global_load_dwordx4 v[16:19], v178, s[46:47] offset:256
	global_load_dwordx4 v[20:23], v178, s[46:47] offset:320
	global_load_dwordx4 v[24:27], v178, s[46:47] offset:384
	global_load_dwordx4 v[28:31], v178, s[46:47] offset:448
	global_load_dwordx4 v[32:35], v178, s[48:49]
	global_load_dwordx4 v[36:39], v178, s[48:49] offset:64
	global_load_dwordx4 v[40:43], v178, s[48:49] offset:128
	global_load_dwordx4 v[44:47], v178, s[48:49] offset:192
	global_load_dwordx4 v[48:51], v178, s[48:49] offset:256
	global_load_dwordx4 v[52:55], v178, s[48:49] offset:320
	global_load_dwordx4 v[56:59], v178, s[48:49] offset:384
	global_load_dwordx4 v[60:63], v178, s[48:49] offset:448
	s_load_dwordx2 s[46:47], s[0:1], 0xc8
	s_load_dwordx2 s[48:49], s[0:1], 0xd8
	s_load_dwordx2 s[40:41], s[0:1], 0xe0
	s_lshl_b32 s50, s10, 8
	s_lshl_b32 s51, s11, 6
	s_add_i32 s50, s50, s51
	s_lshl_b32 s51, s8, 4
	s_add_i32 s50, s50, s51
	v_add_u32_e32 v179, s50, v160
	v_lshlrev_b32_e32 v179, 2, v179
	s_waitcnt lgkmcnt(0)
	global_load_dword v173, v179, s[46:47]
	global_load_dword v174, v179, s[48:49]
	global_load_dword v175, v179, s[40:41]
	v_cmp_gt_u32_e64 s[34:35], 48, v202
	v_cmp_gt_u32_e64 s[36:37], 32, v202
	v_add_u32_e32 v204, 16, v202
	v_add_u32_e32 v205, 32, v202
	v_mov_b32_e32 v206, v160
	s_cmp_eq_u32 s7, 0
	s_cselect_b64 s[38:39], -1, 0
	v_and_b32_e32 v204, 63, v204
	v_lshlrev_b32_e32 v204, 2, v204
	v_and_b32_e32 v205, 63, v205
	v_lshlrev_b32_e32 v205, 2, v205
	v_and_b32_e32 v206, 63, v206
	v_lshlrev_b32_e32 v206, 2, v206
	v_mov_b32_e32 v176, 0
	s_mov_b32 s53, 0xbfb8aa3b
	s_mov_b32 s13, 0
	s_barrier
	s_cmp_lt_u32 s13, 2
	s_sub_i32 s50, 1, s13
	s_lshl_b32 s50, s50, 7
	s_lshl_b32 s51, s9, 8
	s_add_i32 s51, s51, 0x8000
	s_add_i32 s51, s51, s50
	s_sub_i32 s50, 17, s13
	s_lshl_b32 s50, s50, 7
	s_lshl_b32 s59, s9, 11
	s_add_i32 s59, s59, s50
	s_cmp_lt_u32 s13, 2
	s_cselect_b32 s59, s51, s59
	s_lshl_b32 s52, s59, 11
	s_add_u32 s46, s16, s52
	s_addc_u32 s47, s17, 0
	s_lshl_b32 s52, s6, 13
	s_mov_b32 m0, s52
	s_add_i32 s52, s52, 0x400
	global_load_lds_dwordx4 v211, s[46:47]
	s_mov_b32 m0, s52
	s_add_i32 s52, s52, 0x400
	global_load_lds_dwordx4 v212, s[46:47]
	s_mov_b32 m0, s52
	s_add_i32 s52, s52, 0x400
	global_load_lds_dwordx4 v213, s[46:47]
	s_mov_b32 m0, s52
	s_add_i32 s52, s52, 0x400
	global_load_lds_dwordx4 v214, s[46:47]
	s_mov_b32 m0, s52
	s_add_i32 s52, s52, 0x400
	global_load_lds_dwordx4 v215, s[46:47]
	s_mov_b32 m0, s52
	s_add_i32 s52, s52, 0x400
	global_load_lds_dwordx4 v216, s[46:47]
	s_mov_b32 m0, s52
	s_add_i32 s52, s52, 0x400
	global_load_lds_dwordx4 v217, s[46:47]
	s_mov_b32 m0, s52
	s_nop 0
	global_load_lds_dwordx4 v218, s[46:47]
	s_waitcnt vmcnt(8)
	v_mul_f32_e32 v173, s53, v173
	v_mul_f32_e32 v174, s53, v174
	v_mul_f32_e32 v175, s53, v175
	v_exp_f32_e32 v175, v175
	s_nop 0
	v_add_f32_e32 v180, 1.0, v175
	v_log_f32_e32 v180, v180
	v_mov_b32_e32 v181, 0x3eaaaaab
	v_fma_f32 v181, v175, v181, -0.5
	v_fma_f32 v181, v175, v181, 1.0
	v_mul_f32_e32 v181, v175, v181
	v_mul_f32_e32 v181, 0x3fb8aa3b, v181
	v_cmp_gt_f32_e32 vcc, 0x3cf5c28f, v175
	s_nop 1
	v_cndmask_b32_e32 v175, v180, v181, vcc
	v_mul_f32_e32 v175, 0xc1000000, v175
	s_waitcnt vmcnt(0)
	s_barrier
	s_cmp_eq_u32 s13, 17
	s_cbranch_scc1 .Lmylru_nodma_5
	s_add_i32 s58, s13, 1
	s_cmp_lt_u32 s58, 2
	s_sub_i32 s50, 1, s58
	s_lshl_b32 s50, s50, 7
	s_lshl_b32 s51, s9, 8
	s_add_i32 s51, s51, 0x8000
	s_add_i32 s51, s51, s50
	s_sub_i32 s50, 17, s58
	s_lshl_b32 s50, s50, 7
	s_lshl_b32 s59, s9, 11
	s_add_i32 s59, s59, s50
	s_cmp_lt_u32 s58, 2
	s_cselect_b32 s59, s51, s59
	s_lshl_b32 s52, s59, 11
	s_add_u32 s46, s16, s52
	s_addc_u32 s47, s17, 0
	s_lshl_b32 s52, s6, 13
	s_add_i32 s52, s52, 0x10000
	s_mov_b32 m0, s52
	s_add_i32 s52, s52, 0x400
	global_load_lds_dwordx4 v211, s[46:47]
	s_mov_b32 m0, s52
	s_add_i32 s52, s52, 0x400
	global_load_lds_dwordx4 v212, s[46:47]
	s_mov_b32 m0, s52
	s_add_i32 s52, s52, 0x400
	global_load_lds_dwordx4 v213, s[46:47]
	s_mov_b32 m0, s52
	s_add_i32 s52, s52, 0x400
	global_load_lds_dwordx4 v214, s[46:47]
	s_mov_b32 m0, s52
	s_add_i32 s52, s52, 0x400
	global_load_lds_dwordx4 v215, s[46:47]
	s_mov_b32 m0, s52
	s_add_i32 s52, s52, 0x400
	global_load_lds_dwordx4 v216, s[46:47]
	s_mov_b32 m0, s52
	s_add_i32 s52, s52, 0x400
	global_load_lds_dwordx4 v217, s[46:47]
	s_mov_b32 m0, s52
	s_nop 0
	global_load_lds_dwordx4 v218, s[46:47]
